# removed the vmcnt ladder in the accumulator re-zeroing of P6 P7 P10 P11 (it only waited for the epilogue stores)
# speedup vs baseline: 1.0046x; 1.0046x over previous
; template <bool FP8 = false, class Epi, class Sched>
; __device__ __forceinline__ void gemm_phase(LAS unsigned char* lds, const int K, const int lda, const int ldb, const Sched& S, const Epi& E, const int wid) {
;     ...
; #pragma unroll
;         for (int a = 0; a < 2; ++a)
; #pragma unroll
;             for (int b = 0; b < 2; ++b)
; #pragma unroll
;                 for (int m = 0; m < 4; ++m)
; #pragma unroll
;                     for (int n = 0; n < 2; ++n) acc[a][b][m][n] = (f32x4){0.f, 0.f, 0.f, 0.f};
;         cur = nxt; cA = nA; cB = nB; ++ui;
.LBB0_839:
	v_mov_b32_e32 v0, 0
	s_mov_b64 s[56:57], 0
	s_mov_b64 s[50:51], -1
	s_mov_b64 s[54:55], 0
	v_mov_b32_e32 v1, v0
	v_mov_b64_e32 v[2:3], 0
	v_mov_b64_e32 v[4:5], 0
	v_mov_b64_e32 v[6:7], 0
	v_mov_b64_e32 v[16:17], 0
	v_mov_b64_e32 v[18:19], 0
	v_mov_b64_e32 v[20:21], 0
	v_mov_b64_e32 v[22:23], 0
	v_mov_b64_e32 v[32:33], 0
	v_mov_b64_e32 v[34:35], 0
	v_mov_b64_e32 v[36:37], 0
	v_mov_b64_e32 v[38:39], 0
	v_mov_b64_e32 v[56:57], 0
	v_mov_b64_e32 v[58:59], 0
	v_mov_b64_e32 v[60:61], 0
	v_mov_b64_e32 v[62:63], 0
	v_mov_b64_e32 v[8:9], 0
	v_mov_b64_e32 v[10:11], 0
	v_mov_b64_e32 v[12:13], 0
	v_mov_b64_e32 v[14:15], 0
	v_mov_b64_e32 v[24:25], 0
	v_mov_b64_e32 v[26:27], 0
	v_mov_b64_e32 v[28:29], 0
	v_mov_b64_e32 v[30:31], 0
	v_mov_b64_e32 v[48:49], 0
	v_mov_b64_e32 v[50:51], 0
	v_mov_b64_e32 v[52:53], 0
	v_mov_b64_e32 v[54:55], 0
	v_mov_b64_e32 v[72:73], 0
	v_mov_b64_e32 v[74:75], 0
	v_mov_b64_e32 v[76:77], 0
	v_mov_b64_e32 v[78:79], 0
	v_mov_b64_e32 v[80:81], 0
	v_mov_b64_e32 v[82:83], 0
	v_mov_b64_e32 v[84:85], 0
	v_mov_b64_e32 v[86:87], 0
	v_mov_b64_e32 v[96:97], 0
	v_mov_b64_e32 v[98:99], 0
	v_mov_b64_e32 v[100:101], 0
	v_mov_b64_e32 v[102:103], 0
	v_mov_b64_e32 v[112:113], 0
	v_mov_b64_e32 v[114:115], 0
	v_mov_b64_e32 v[116:117], 0
	v_mov_b64_e32 v[118:119], 0
	v_mov_b64_e32 v[128:129], 0
	v_mov_b64_e32 v[130:131], 0
	v_mov_b64_e32 v[132:133], 0
	v_mov_b64_e32 v[134:135], 0
	v_mov_b64_e32 v[88:89], 0
	v_mov_b32_e32 v90, v0
	v_mov_b32_e32 v91, v0
	v_mov_b32_e32 v92, v0
	v_mov_b32_e32 v93, v0
	v_mov_b32_e32 v94, v0
	v_mov_b32_e32 v95, v0
	v_mov_b32_e32 v104, v0
	v_mov_b32_e32 v105, v0
	v_mov_b32_e32 v106, v0
	v_mov_b32_e32 v107, v0
	v_mov_b32_e32 v108, v0
	v_mov_b32_e32 v109, v0
	v_mov_b32_e32 v110, v0
	v_mov_b32_e32 v111, v0
	v_mov_b32_e32 v120, v0
	v_mov_b32_e32 v121, v0
	v_mov_b32_e32 v122, v0
	v_mov_b32_e32 v123, v0
	v_mov_b32_e32 v124, v0
	v_mov_b32_e32 v125, v0
	v_mov_b32_e32 v126, v0
	v_mov_b32_e32 v127, v0
	v_mov_b32_e32 v136, v0
	v_mov_b32_e32 v137, v0
	v_mov_b32_e32 v138, v0
	v_mov_b32_e32 v139, v0
	v_mov_b32_e32 v140, v0
	v_mov_b32_e32 v141, v0
	v_mov_b32_e32 v142, v0
	v_mov_b32_e32 v143, v0

; template <bool FP8 = false, class Epi, class Sched>
; __device__ __forceinline__ void gemm_phase(LAS unsigned char* lds, const int K, const int lda, const int ldb, const Sched& S, const Epi& E, const int wid) {
;     ...
; #pragma unroll
;         for (int a = 0; a < 2; ++a)
; #pragma unroll
;             for (int b = 0; b < 2; ++b)
; #pragma unroll
;                 for (int m = 0; m < 4; ++m)
; #pragma unroll
;                     for (int n = 0; n < 2; ++n) acc[a][b][m][n] = (f32x4){0.f, 0.f, 0.f, 0.f};
;         cur = nxt; cA = nA; cB = nB; ++ui;
.LBB0_917:
	s_add_u32 s43, s56, 0x100
	v_mov_b32_e32 v0, 0
	s_addc_u32 s69, s57, 0
	s_mov_b32 s70, -2
	v_mov_b32_e32 v1, v0
	v_mov_b64_e32 v[2:3], 0
	v_mov_b64_e32 v[4:5], 0
	v_mov_b64_e32 v[6:7], 0
	v_mov_b64_e32 v[16:17], 0
	v_mov_b64_e32 v[18:19], 0
	v_mov_b64_e32 v[20:21], 0
	v_mov_b64_e32 v[22:23], 0
	v_mov_b64_e32 v[32:33], 0
	v_mov_b64_e32 v[34:35], 0
	v_mov_b64_e32 v[36:37], 0
	v_mov_b64_e32 v[38:39], 0
	v_mov_b64_e32 v[48:49], 0
	v_mov_b64_e32 v[50:51], 0
	v_mov_b64_e32 v[52:53], 0
	v_mov_b64_e32 v[54:55], 0
	v_mov_b64_e32 v[8:9], 0
	v_mov_b64_e32 v[10:11], 0
	v_mov_b64_e32 v[12:13], 0
	v_mov_b64_e32 v[14:15], 0
	v_mov_b64_e32 v[24:25], 0
	v_mov_b64_e32 v[26:27], 0
	v_mov_b64_e32 v[28:29], 0
	v_mov_b64_e32 v[30:31], 0
	v_mov_b64_e32 v[40:41], 0
	v_mov_b64_e32 v[42:43], 0
	v_mov_b64_e32 v[44:45], 0
	v_mov_b64_e32 v[46:47], 0
	v_mov_b64_e32 v[56:57], 0
	v_mov_b64_e32 v[58:59], 0
	v_mov_b64_e32 v[60:61], 0
	v_mov_b64_e32 v[62:63], 0
	v_mov_b64_e32 v[64:65], 0
	v_mov_b64_e32 v[66:67], 0
	v_mov_b64_e32 v[68:69], 0
	v_mov_b64_e32 v[70:71], 0
	v_mov_b64_e32 v[80:81], 0
	v_mov_b64_e32 v[82:83], 0
	v_mov_b64_e32 v[84:85], 0
	v_mov_b64_e32 v[86:87], 0
	v_mov_b64_e32 v[104:105], 0
	v_mov_b64_e32 v[106:107], 0
	v_mov_b64_e32 v[108:109], 0
	v_mov_b64_e32 v[110:111], 0
	v_mov_b64_e32 v[128:129], 0
	v_mov_b64_e32 v[130:131], 0
	v_mov_b64_e32 v[132:133], 0
	v_mov_b64_e32 v[134:135], 0
	v_mov_b64_e32 v[72:73], 0
	v_mov_b32_e32 v74, v0
	v_mov_b32_e32 v75, v0
	v_mov_b32_e32 v76, v0
	v_mov_b32_e32 v77, v0
	v_mov_b32_e32 v78, v0
	v_mov_b32_e32 v79, v0
	v_mov_b32_e32 v88, v0
	v_mov_b32_e32 v89, v0
	v_mov_b32_e32 v90, v0
	v_mov_b32_e32 v91, v0
	v_mov_b32_e32 v92, v0
	v_mov_b32_e32 v93, v0
	v_mov_b32_e32 v94, v0
	v_mov_b32_e32 v95, v0
	v_mov_b32_e32 v120, v0
	v_mov_b32_e32 v121, v0
	v_mov_b32_e32 v122, v0
	v_mov_b32_e32 v123, v0
	v_mov_b32_e32 v124, v0
	v_mov_b32_e32 v125, v0
	v_mov_b32_e32 v126, v0
	v_mov_b32_e32 v127, v0
	v_mov_b32_e32 v136, v0
	v_mov_b32_e32 v137, v0
	v_mov_b32_e32 v138, v0
	v_mov_b32_e32 v139, v0
	v_mov_b32_e32 v140, v0
	v_mov_b32_e32 v141, v0
	v_mov_b32_e32 v142, v0
	v_mov_b32_e32 v143, v0

; template <bool FP8 = false, class Epi, class Sched>
; __device__ __forceinline__ void gemm_phase(LAS unsigned char* lds, const int K, const int lda, const int ldb, const Sched& S, const Epi& E, const int wid) {
;     ...
; #pragma unroll
;         for (int a = 0; a < 2; ++a)
; #pragma unroll
;             for (int b = 0; b < 2; ++b)
; #pragma unroll
;                 for (int m = 0; m < 4; ++m)
; #pragma unroll
;                     for (int n = 0; n < 2; ++n) acc[a][b][m][n] = (f32x4){0.f, 0.f, 0.f, 0.f};
;         cur = nxt; cA = nA; cB = nB; ++ui;
.LBB0_1058:
	s_add_u32 s39, s56, 0x100
	v_mov_b32_e32 v0, 0
	s_addc_u32 s43, s57, 0
	s_mov_b32 s49, -2
	v_mov_b32_e32 v1, v0
	v_mov_b64_e32 v[2:3], 0
	v_mov_b64_e32 v[4:5], 0
	v_mov_b64_e32 v[6:7], 0
	v_mov_b64_e32 v[16:17], 0
	v_mov_b64_e32 v[18:19], 0
	v_mov_b64_e32 v[20:21], 0
	v_mov_b64_e32 v[22:23], 0
	v_mov_b64_e32 v[32:33], 0
	v_mov_b64_e32 v[34:35], 0
	v_mov_b64_e32 v[36:37], 0
	v_mov_b64_e32 v[38:39], 0
	v_mov_b64_e32 v[48:49], 0
	v_mov_b64_e32 v[50:51], 0
	v_mov_b64_e32 v[52:53], 0
	v_mov_b64_e32 v[54:55], 0
	v_mov_b64_e32 v[8:9], 0
	v_mov_b64_e32 v[10:11], 0
	v_mov_b64_e32 v[12:13], 0
	v_mov_b64_e32 v[14:15], 0
	v_mov_b64_e32 v[24:25], 0
	v_mov_b64_e32 v[26:27], 0
	v_mov_b64_e32 v[28:29], 0
	v_mov_b64_e32 v[30:31], 0
	v_mov_b64_e32 v[40:41], 0
	v_mov_b64_e32 v[42:43], 0
	v_mov_b64_e32 v[44:45], 0
	v_mov_b64_e32 v[46:47], 0
	v_mov_b64_e32 v[56:57], 0
	v_mov_b64_e32 v[58:59], 0
	v_mov_b64_e32 v[60:61], 0
	v_mov_b64_e32 v[62:63], 0
	v_mov_b64_e32 v[64:65], 0
	v_mov_b64_e32 v[66:67], 0
	v_mov_b64_e32 v[68:69], 0
	v_mov_b64_e32 v[70:71], 0
	v_mov_b64_e32 v[96:97], 0
	v_mov_b64_e32 v[98:99], 0
	v_mov_b64_e32 v[100:101], 0
	v_mov_b64_e32 v[102:103], 0
	v_mov_b64_e32 v[112:113], 0
	v_mov_b64_e32 v[114:115], 0
	v_mov_b64_e32 v[116:117], 0
	v_mov_b64_e32 v[118:119], 0
	v_mov_b64_e32 v[128:129], 0
	v_mov_b64_e32 v[130:131], 0
	v_mov_b64_e32 v[132:133], 0
	v_mov_b64_e32 v[134:135], 0
	v_mov_b64_e32 v[72:73], 0
	v_mov_b32_e32 v74, v0
	v_mov_b32_e32 v75, v0
	v_mov_b32_e32 v76, v0
	v_mov_b32_e32 v77, v0
	v_mov_b32_e32 v78, v0
	v_mov_b32_e32 v79, v0
	v_mov_b32_e32 v104, v0
	v_mov_b32_e32 v105, v0
	v_mov_b32_e32 v106, v0
	v_mov_b32_e32 v107, v0
	v_mov_b32_e32 v108, v0
	v_mov_b32_e32 v109, v0
	v_mov_b32_e32 v110, v0
	v_mov_b32_e32 v111, v0
	v_mov_b32_e32 v120, v0
	v_mov_b32_e32 v121, v0
	v_mov_b32_e32 v122, v0
	v_mov_b32_e32 v123, v0
	v_mov_b32_e32 v124, v0
	v_mov_b32_e32 v125, v0
	v_mov_b32_e32 v126, v0
	v_mov_b32_e32 v127, v0
	v_mov_b32_e32 v136, v0
	v_mov_b32_e32 v137, v0
	v_mov_b32_e32 v138, v0
	v_mov_b32_e32 v139, v0
	v_mov_b32_e32 v140, v0
	v_mov_b32_e32 v141, v0
	v_mov_b32_e32 v142, v0
	v_mov_b32_e32 v143, v0

; template <bool FP8 = false, class Epi, class Sched>
; __device__ __forceinline__ void gemm_phase(LAS unsigned char* lds, const int K, const int lda, const int ldb, const Sched& S, const Epi& E, const int wid) {
;     ...
; #pragma unroll
;         for (int a = 0; a < 2; ++a)
; #pragma unroll
;             for (int b = 0; b < 2; ++b)
; #pragma unroll
;                 for (int m = 0; m < 4; ++m)
; #pragma unroll
;                     for (int n = 0; n < 2; ++n) acc[a][b][m][n] = (f32x4){0.f, 0.f, 0.f, 0.f};
;         cur = nxt; cA = nA; cB = nB; ++ui;
.LBB0_1132:
	s_add_u32 s45, s66, 0x100
	v_mov_b32_e32 v0, 0
	s_addc_u32 s49, s67, 0
	s_mov_b32 s51, -2
	v_mov_b32_e32 v1, v0
	v_mov_b64_e32 v[2:3], 0
	v_mov_b64_e32 v[4:5], 0
	v_mov_b64_e32 v[6:7], 0
	v_mov_b64_e32 v[16:17], 0
	v_mov_b64_e32 v[18:19], 0
	v_mov_b64_e32 v[20:21], 0
	v_mov_b64_e32 v[22:23], 0
	v_mov_b64_e32 v[32:33], 0
	v_mov_b64_e32 v[34:35], 0
	v_mov_b64_e32 v[36:37], 0
	v_mov_b64_e32 v[38:39], 0
	v_mov_b64_e32 v[48:49], 0
	v_mov_b64_e32 v[50:51], 0
	v_mov_b64_e32 v[52:53], 0
	v_mov_b64_e32 v[54:55], 0
	v_mov_b64_e32 v[8:9], 0
	v_mov_b64_e32 v[10:11], 0
	v_mov_b64_e32 v[12:13], 0
	v_mov_b64_e32 v[14:15], 0
	v_mov_b64_e32 v[24:25], 0
	v_mov_b64_e32 v[26:27], 0
	v_mov_b64_e32 v[28:29], 0
	v_mov_b64_e32 v[30:31], 0
	v_mov_b64_e32 v[40:41], 0
	v_mov_b64_e32 v[42:43], 0
	v_mov_b64_e32 v[44:45], 0
	v_mov_b64_e32 v[46:47], 0
	v_mov_b64_e32 v[56:57], 0
	v_mov_b64_e32 v[58:59], 0
	v_mov_b64_e32 v[60:61], 0
	v_mov_b64_e32 v[62:63], 0
	v_mov_b64_e32 v[64:65], 0
	v_mov_b64_e32 v[66:67], 0
	v_mov_b64_e32 v[68:69], 0
	v_mov_b64_e32 v[70:71], 0
	v_mov_b64_e32 v[80:81], 0
	v_mov_b64_e32 v[82:83], 0
	v_mov_b64_e32 v[84:85], 0
	v_mov_b64_e32 v[86:87], 0
	v_mov_b64_e32 v[96:97], 0
	v_mov_b64_e32 v[98:99], 0
	v_mov_b64_e32 v[100:101], 0
	v_mov_b64_e32 v[102:103], 0
	v_mov_b64_e32 v[112:113], 0
	v_mov_b64_e32 v[114:115], 0
	v_mov_b64_e32 v[116:117], 0
	v_mov_b64_e32 v[118:119], 0
	v_mov_b64_e32 v[72:73], 0
	v_mov_b32_e32 v74, v0
	v_mov_b32_e32 v75, v0
	v_mov_b32_e32 v76, v0
	v_mov_b32_e32 v77, v0
	v_mov_b32_e32 v78, v0
	v_mov_b32_e32 v79, v0
	v_mov_b32_e32 v88, v0
	v_mov_b32_e32 v89, v0
	v_mov_b32_e32 v90, v0
	v_mov_b32_e32 v91, v0
	v_mov_b32_e32 v92, v0
	v_mov_b32_e32 v93, v0
	v_mov_b32_e32 v94, v0
	v_mov_b32_e32 v95, v0
	v_mov_b32_e32 v104, v0
	v_mov_b32_e32 v105, v0
	v_mov_b32_e32 v106, v0
	v_mov_b32_e32 v107, v0
	v_mov_b32_e32 v108, v0
	v_mov_b32_e32 v109, v0
	v_mov_b32_e32 v110, v0
	v_mov_b32_e32 v111, v0
	v_mov_b32_e32 v120, v0
	v_mov_b32_e32 v121, v0
	v_mov_b32_e32 v122, v0
	v_mov_b32_e32 v123, v0
	v_mov_b32_e32 v124, v0
	v_mov_b32_e32 v125, v0
	v_mov_b32_e32 v126, v0
	v_mov_b32_e32 v127, v0
